# DeltaNet recurrence: counted LDS waits that no longer have anything to wait for removed; one full LDS wait in front of the first reader of the few remaining ds_bpermute results
# speedup vs baseline: 1.0091x; 1.0091x over previous
.LBB0_799:
	s_ashr_i32 s4, s16, 1
	s_lshl_b32 s20, s4, 6
	s_and_b32 s17, s4, 3
	s_and_b32 s4, s20, 0xffffff00
	s_or_b32 s14, s4, s17
	s_ashr_i32 s15, s14, 31
	s_lshl_b64 s[4:5], s[14:15], 13
	v_readlane_b32 s6, v253, 22
	v_lshl_add_u64 v[20:21], v[134:135], 0, s[4:5]
	v_readlane_b32 s7, v253, 23
	s_add_u32 s4, s6, s4
	s_addc_u32 s5, s7, s5
	s_lshl_b32 s6, s16, 11
	s_and_b32 s6, s6, 0x800
	v_or_b32_e32 v36, s6, v132
	v_lshlrev_b32_e32 v2, 1, v132
	v_mov_b32_e32 v143, v3
	v_mov_b32_e32 v37, v3
	v_lshlrev_b32_e32 v36, 1, v36
	v_lshl_add_u64 v[16:17], v[20:21], 0, v[2:3]
	v_lshl_add_u64 v[32:33], v[20:21], 0, v[142:143]
	v_mov_b32_e32 v145, v3
	v_lshl_add_u64 v[38:39], s[4:5], 0, v[36:37]
	global_load_dwordx4 v[4:7], v[16:17], off
	global_load_dwordx4 v[8:11], v[16:17], off offset:32
	global_load_dwordx4 v[12:15], v[16:17], off offset:64
	v_lshl_add_u64 v[38:39], v[38:39], 0, v[144:145]
	global_load_dwordx4 v[16:19], v[16:17], off offset:96
	s_nop 0
	global_load_dwordx4 v[20:23], v[32:33], off
	global_load_dwordx4 v[24:27], v[32:33], off offset:32
	global_load_dwordx4 v[28:31], v[32:33], off offset:64
	s_nop 0
	global_load_dwordx4 v[32:35], v[32:33], off offset:96
	s_nop 0
	global_load_dwordx2 v[158:159], v[38:39], off
	global_load_dwordx2 v[154:155], v[38:39], off offset:16
	global_load_dwordx2 v[152:153], v[38:39], off offset:32
	global_load_dwordx2 v[150:151], v[38:39], off offset:48
	global_load_dwordx2 v[164:165], v[38:39], off offset:64
	global_load_dwordx2 v[162:163], v[38:39], off offset:80
	global_load_dwordx2 v[160:161], v[38:39], off offset:96
	global_load_dwordx2 v[156:157], v[38:39], off offset:112
	v_lshl_add_u64 v[146:147], v[138:139], 0, v[36:37]
	v_lshl_add_u64 v[148:149], v[140:141], 0, v[36:37]
	s_mov_b32 s15, 0
	s_waitcnt vmcnt(0)
	v_cndmask_b32_e32 v38, v4, v6, vcc
	ds_bpermute_b32 v38, v166, v38
	s_waitcnt lgkmcnt(0)
	v_cndmask_b32_e32 v92, v38, v4, vcc
	v_mov_b32_e32 v4, 0
	v_mov_b32_e32 v93, v5
	v_mov_b32_e32 v95, v7
	s_nop 3
	v_permlane32_swap_b32_e32 v93, v95
	s_nop 1
	v_cndmask_b32_e32 v94, v6, v38, vcc
	v_mov_b64_e32 v[76:77], v[8:9]
	v_mov_b64_e32 v[78:79], v[10:11]
	s_nop 3
	v_permlane32_swap_b32_e32 v77, v79
	v_permlane32_swap_b32_e32 v76, v78
	s_nop 1
	v_mov_b64_e32 v[84:85], v[12:13]
	v_mov_b64_e32 v[86:87], v[14:15]
	s_nop 3
	v_permlane32_swap_b32_e32 v85, v87
	v_permlane32_swap_b32_e32 v84, v86
	s_nop 1
	v_mov_b64_e32 v[68:69], v[16:17]
	v_mov_b64_e32 v[70:71], v[18:19]
	s_nop 3
	v_permlane32_swap_b32_e32 v69, v71
	v_permlane32_swap_b32_e32 v68, v70
	s_nop 1
	v_mov_b64_e32 v[96:97], v[20:21]
	v_mov_b64_e32 v[98:99], v[22:23]
	s_nop 3
	v_permlane32_swap_b32_e32 v97, v99
	v_permlane32_swap_b32_e32 v96, v98
	s_nop 1
	v_mov_b64_e32 v[80:81], v[24:25]
	v_mov_b64_e32 v[82:83], v[26:27]
	s_nop 3
	v_permlane32_swap_b32_e32 v81, v83
	v_permlane32_swap_b32_e32 v80, v82
	s_nop 1
	v_mov_b64_e32 v[88:89], v[28:29]
	v_mov_b64_e32 v[90:91], v[30:31]
	s_nop 3
	v_permlane32_swap_b32_e32 v89, v91
	v_permlane32_swap_b32_e32 v88, v90
	s_nop 1
	s_waitcnt lgkmcnt(0)
	v_mov_b64_e32 v[72:73], v[32:33]
	v_mov_b64_e32 v[74:75], v[34:35]
	s_nop 3
	v_permlane32_swap_b32_e32 v73, v75
	v_permlane32_swap_b32_e32 v72, v74
	s_nop 1
	v_mov_b32_e32 v5, v4
	v_mov_b32_e32 v6, v4
	v_mov_b32_e32 v7, v4
	v_mov_b32_e32 v8, v4
	v_mov_b32_e32 v9, v4
	v_mov_b32_e32 v10, v4
	v_mov_b32_e32 v11, v4
	v_mov_b32_e32 v12, v4
	v_mov_b32_e32 v13, v4
	v_mov_b32_e32 v14, v4
	v_mov_b32_e32 v15, v4
	v_mov_b32_e32 v16, v4
	v_mov_b32_e32 v17, v4
	v_mov_b32_e32 v18, v4
	v_mov_b32_e32 v19, v4
	v_mov_b32_e32 v20, v4
	v_mov_b32_e32 v21, v4
	v_mov_b32_e32 v22, v4
	v_mov_b32_e32 v23, v4
	v_mov_b32_e32 v24, v4
	v_mov_b32_e32 v25, v4
	v_mov_b32_e32 v26, v4
	v_mov_b32_e32 v27, v4
	v_mov_b32_e32 v28, v4
	v_mov_b32_e32 v29, v4
	v_mov_b32_e32 v30, v4
	v_mov_b32_e32 v31, v4
	v_mov_b32_e32 v32, v4
	v_mov_b32_e32 v33, v4
	v_mov_b32_e32 v34, v4
	v_mov_b32_e32 v35, v4
.LBB0_800:
	v_lshlrev_b32_e32 v36, 16, v158
	v_and_b32_e32 v37, 0xffff0000, v158
	v_lshlrev_b32_e32 v38, 16, v159
	v_and_b32_e32 v39, 0xffff0000, v159
	v_lshlrev_b32_e32 v40, 16, v154
	v_and_b32_e32 v41, 0xffff0000, v154
	v_lshlrev_b32_e32 v42, 16, v155
	v_and_b32_e32 v43, 0xffff0000, v155
	v_lshlrev_b32_e32 v44, 16, v152
	v_and_b32_e32 v45, 0xffff0000, v152
	v_lshlrev_b32_e32 v46, 16, v153
	v_and_b32_e32 v47, 0xffff0000, v153
	v_lshlrev_b32_e32 v48, 16, v150
	v_and_b32_e32 v49, 0xffff0000, v150
	v_lshlrev_b32_e32 v50, 16, v151
	v_and_b32_e32 v51, 0xffff0000, v151
	v_cvt_pk_bf16_f32 v116, -v20, -v21
	v_cvt_pk_bf16_f32 v117, -v22, -v23
	v_cvt_pk_bf16_f32 v118, -v24, -v25
	v_cvt_pk_bf16_f32 v119, -v26, -v27
	v_lshlrev_b32_e32 v52, 16, v164
	v_and_b32_e32 v53, 0xffff0000, v164
	v_mfma_f32_32x32x16_bf16 v[36:51], v[92:95], v[116:119], v[36:51]
	v_lshlrev_b32_e32 v54, 16, v165
	v_and_b32_e32 v55, 0xffff0000, v165
	v_lshlrev_b32_e32 v56, 16, v162
	v_and_b32_e32 v57, 0xffff0000, v162
	v_lshlrev_b32_e32 v58, 16, v163
	v_and_b32_e32 v59, 0xffff0000, v163
	v_lshlrev_b32_e32 v60, 16, v160
	v_and_b32_e32 v61, 0xffff0000, v160
	v_lshlrev_b32_e32 v62, 16, v161
	v_and_b32_e32 v63, 0xffff0000, v161
	v_lshlrev_b32_e32 v64, 16, v156
	v_and_b32_e32 v65, 0xffff0000, v156
	v_lshlrev_b32_e32 v66, 16, v157
	v_and_b32_e32 v67, 0xffff0000, v157
	s_add_i32 s18, s14, s15
	s_ashr_i32 s19, s18, 31
	v_mfma_f32_32x32x16_bf16 v[52:67], v[96:99], v[116:119], v[52:67]
	s_lshl_b64 s[4:5], s[18:19], 2
	v_cvt_pk_bf16_f32 v120, -v4, -v5
	v_cvt_pk_bf16_f32 v121, -v6, -v7
	v_cvt_pk_bf16_f32 v122, -v8, -v9
	v_cvt_pk_bf16_f32 v123, -v10, -v11
	s_add_u32 s8, s12, s4
	s_addc_u32 s9, s13, s5
	s_lshl_b64 s[6:7], s[18:19], 13
	v_mfma_f32_32x32x16_bf16 v[36:51], v[84:87], v[120:123], v[36:51]
	v_lshl_add_u64 v[96:97], v[136:137], 0, s[6:7]
	v_cvt_pk_bf16_f32 v124, -v28, -v29
	v_cvt_pk_bf16_f32 v125, -v30, -v31
	v_lshl_add_u64 v[150:151], v[96:97], 0, v[2:3]
	v_mfma_f32_32x32x16_bf16 v[52:67], v[88:91], v[120:123], v[52:67]
	v_cvt_pk_bf16_f32 v126, -v32, -v33
	global_load_dword v204, v3, s[8:9]
	v_lshl_add_u64 v[152:153], v[96:97], 0, v[142:143]
	global_load_dwordx4 v[96:99], v[150:151], off
	global_load_dwordx4 v[116:119], v[150:151], off offset:32
	s_add_i32 s4, s18, 4
	s_ashr_i32 s5, s4, 31
	s_lshl_b64 s[4:5], s[4:5], 13
	v_cvt_pk_bf16_f32 v127, -v34, -v35
	global_load_dwordx4 v[84:87], v[152:153], off
	global_load_dwordx4 v[128:131], v[152:153], off offset:32
	global_load_dwordx4 v[168:171], v[150:151], off offset:64
	global_load_dwordx4 v[172:175], v[150:151], off offset:96
	global_load_dwordx4 v[176:179], v[152:153], off offset:64
	global_load_dwordx4 v[180:183], v[152:153], off offset:96
	v_lshl_add_u64 v[150:151], v[134:135], 0, s[4:5]
	v_lshl_add_u64 v[88:89], v[146:147], 0, s[4:5]
	v_cvt_pk_bf16_f32 v92, -v12, -v13
	v_cvt_pk_bf16_f32 v93, -v14, -v15
	v_cvt_pk_bf16_f32 v94, -v16, -v17
	v_cvt_pk_bf16_f32 v95, -v18, -v19
	v_lshl_add_u64 v[120:121], v[150:151], 0, v[2:3]
	v_lshl_add_u64 v[196:197], v[150:151], 0, v[142:143]
	global_load_dwordx2 v[158:159], v[88:89], off
	global_load_dwordx2 v[154:155], v[88:89], off offset:16
	global_load_dwordx2 v[152:153], v[88:89], off offset:32
	v_mfma_f32_32x32x16_bf16 v[36:51], v[76:79], v[124:127], v[36:51]
	global_load_dwordx2 v[150:151], v[88:89], off offset:48
	global_load_dwordx2 v[164:165], v[88:89], off offset:64
	global_load_dwordx2 v[162:163], v[88:89], off offset:80
	global_load_dwordx2 v[160:161], v[88:89], off offset:96
	global_load_dwordx2 v[156:157], v[88:89], off offset:112
	global_load_dwordx4 v[76:79], v[120:121], off
	s_nop 0
	global_load_dwordx4 v[88:91], v[120:121], off offset:32
	v_cvt_pk_bf16_f32 v100, v20, v21
	v_cvt_pk_bf16_f32 v101, v22, v23
	v_cvt_pk_bf16_f32 v102, v4, v5
	v_cvt_pk_bf16_f32 v103, v6, v7
	v_cvt_pk_bf16_f32 v104, v24, v25
	v_cvt_pk_bf16_f32 v105, v26, v27
	v_mfma_f32_32x32x16_bf16 v[52:67], v[80:83], v[124:127], v[52:67]
	global_load_dwordx4 v[80:83], v[120:121], off offset:64
	s_nop 0
	global_load_dwordx4 v[120:123], v[120:121], off offset:96
	s_nop 0
	global_load_dwordx4 v[184:187], v[196:197], off
	global_load_dwordx4 v[188:191], v[196:197], off offset:32
	global_load_dwordx4 v[192:195], v[196:197], off offset:64
	s_nop 0
	global_load_dwordx4 v[196:199], v[196:197], off offset:96
	v_lshl_add_u64 v[206:207], v[148:149], 0, s[6:7]
	v_cvt_pk_bf16_f32 v106, v8, v9
	v_cvt_pk_bf16_f32 v107, v10, v11
	v_cvt_pk_bf16_f32 v108, v28, v29
	v_cvt_pk_bf16_f32 v109, v30, v31
	v_cvt_pk_bf16_f32 v110, v12, v13
	v_mfma_f32_32x32x16_bf16 v[36:51], v[68:71], v[92:95], v[36:51]
	v_cvt_pk_bf16_f32 v111, v14, v15
	v_cvt_pk_bf16_f32 v112, v32, v33
	v_cvt_pk_bf16_f32 v113, v34, v35
	v_cvt_pk_bf16_f32 v114, v16, v17
	v_cvt_pk_bf16_f32 v115, v18, v19
	global_store_dwordx2 v[206:207], v[100:101], off
	global_store_dwordx2 v[206:207], v[102:103], off offset:64
	global_store_dwordx2 v[206:207], v[104:105], off offset:16
	global_store_dwordx2 v[206:207], v[106:107], off offset:80
	global_store_dwordx2 v[206:207], v[108:109], off offset:32
	global_store_dwordx2 v[206:207], v[110:111], off offset:96
	global_store_dwordx2 v[206:207], v[112:113], off offset:48
	global_store_dwordx2 v[206:207], v[114:115], off offset:112
	v_mfma_f32_32x32x16_bf16 v[52:67], v[72:75], v[92:95], v[52:67]
	v_cvt_pk_bf16_f32 v36, v36, v37
	v_cvt_pk_bf16_f32 v37, v38, v39
	v_cvt_pk_bf16_f32 v39, v42, v43
	v_cvt_pk_bf16_f32 v42, v48, v49
	v_cvt_pk_bf16_f32 v38, v40, v41
	v_cvt_pk_bf16_f32 v40, v44, v45
	v_cvt_pk_bf16_f32 v43, v50, v51
	s_nop 4
	v_cvt_pk_bf16_f32 v52, v52, v53
	v_cvt_pk_bf16_f32 v53, v54, v55
	v_cvt_pk_bf16_f32 v54, v56, v57
	v_cvt_pk_bf16_f32 v44, v60, v61
	v_cvt_pk_bf16_f32 v45, v62, v63
	v_cvt_pk_bf16_f32 v41, v46, v47
	v_cvt_pk_bf16_f32 v46, v64, v65
	v_lshl_add_u64 v[208:209], v[146:147], 0, s[6:7]
	v_cvt_pk_bf16_f32 v55, v58, v59
	v_cvt_pk_bf16_f32 v47, v66, v67
	global_store_dwordx2 v[208:209], v[36:37], off
	global_store_dwordx2 v[208:209], v[52:53], off offset:64
	global_store_dwordx2 v[208:209], v[38:39], off offset:16
	global_store_dwordx2 v[208:209], v[54:55], off offset:80
	global_store_dwordx2 v[208:209], v[40:41], off offset:32
	global_store_dwordx2 v[208:209], v[44:45], off offset:96
	global_store_dwordx2 v[208:209], v[42:43], off offset:48
	global_store_dwordx2 v[208:209], v[46:47], off offset:112
	s_add_i32 s15, s15, 4
	s_cmpk_lg_i32 s15, 0xfc
	s_waitcnt vmcnt(40)
	v_pk_mul_f32 v[34:35], v[34:35], v[204:205] op_sel_hi:[1,0]
	s_waitcnt vmcnt(39)
	s_waitcnt vmcnt(38)
	v_pk_mul_f32 v[32:33], v[32:33], v[204:205] op_sel_hi:[1,0]
	v_pk_mul_f32 v[30:31], v[30:31], v[204:205] op_sel_hi:[1,0]
	v_pk_mul_f32 v[28:29], v[28:29], v[204:205] op_sel_hi:[1,0]
	s_waitcnt vmcnt(37)
	s_waitcnt vmcnt(35)
	s_waitcnt vmcnt(34)
	v_pk_mul_f32 v[26:27], v[26:27], v[204:205] op_sel_hi:[1,0]
	v_pk_mul_f32 v[24:25], v[24:25], v[204:205] op_sel_hi:[1,0]
	v_pk_mul_f32 v[22:23], v[22:23], v[204:205] op_sel_hi:[1,0]
	s_waitcnt vmcnt(23)
	v_pk_mul_f32 v[20:21], v[20:21], v[204:205] op_sel_hi:[1,0]
	v_pk_mul_f32 v[18:19], v[18:19], v[204:205] op_sel_hi:[1,0]
	v_pk_mul_f32 v[16:17], v[16:17], v[204:205] op_sel_hi:[1,0]
	s_waitcnt vmcnt(20)
	v_cndmask_b32_e32 v60, v120, v122, vcc
	v_cndmask_b32_e32 v61, v121, v123, vcc
	s_waitcnt vmcnt(19)
	v_cndmask_b32_e32 v62, v184, v186, vcc
	v_cndmask_b32_e32 v63, v185, v187, vcc
	v_pk_mul_f32 v[14:15], v[14:15], v[204:205] op_sel_hi:[1,0]
	v_pk_mul_f32 v[12:13], v[12:13], v[204:205] op_sel_hi:[1,0]
	v_pk_mul_f32 v[10:11], v[10:11], v[204:205] op_sel_hi:[1,0]
	v_pk_mul_f32 v[8:9], v[8:9], v[204:205] op_sel_hi:[1,0]
	v_pk_mul_f32 v[6:7], v[6:7], v[204:205] op_sel_hi:[1,0]
	v_pk_mul_f32 v[4:5], v[4:5], v[204:205] op_sel_hi:[1,0]
	ds_bpermute_b32 v145, v166, v60
	ds_bpermute_b32 v167, v166, v61
	ds_bpermute_b32 v203, v166, v62
	ds_bpermute_b32 v204, v166, v63
	v_mov_b64_e32 v[48:49], v[96:97]
	v_mov_b64_e32 v[50:51], v[98:99]
	s_nop 3
	v_permlane32_swap_b32_e32 v49, v51
	v_permlane32_swap_b32_e32 v48, v50
	s_nop 1
	v_mov_b64_e32 v[60:61], v[84:85]
	v_mov_b64_e32 v[62:63], v[86:87]
	s_nop 3
	v_permlane32_swap_b32_e32 v61, v63
	v_permlane32_swap_b32_e32 v60, v62
	s_nop 1
	v_mfma_f32_32x32x16_bf16 v[20:35], v[48:51], v[36:39], v[20:35]
	v_mov_b64_e32 v[48:49], v[168:169]
	v_mov_b64_e32 v[50:51], v[170:171]
	s_nop 3
	v_permlane32_swap_b32_e32 v49, v51
	v_permlane32_swap_b32_e32 v48, v50
	s_nop 1
	v_mfma_f32_32x32x16_bf16 v[4:19], v[60:63], v[36:39], v[4:19]
	v_mov_b64_e32 v[36:37], v[176:177]
	v_mov_b64_e32 v[38:39], v[178:179]
	s_nop 3
	v_permlane32_swap_b32_e32 v37, v39
	v_permlane32_swap_b32_e32 v36, v38
	s_nop 1
	v_mfma_f32_32x32x16_bf16 v[20:35], v[48:51], v[52:55], v[20:35]
	s_waitcnt vmcnt(18)
	v_mfma_f32_32x32x16_bf16 v[4:19], v[36:39], v[52:55], v[4:19]
	s_waitcnt vmcnt(17)
	v_mov_b64_e32 v[56:57], v[116:117]
	v_mov_b64_e32 v[58:59], v[118:119]
	s_nop 3
	v_permlane32_swap_b32_e32 v57, v59
	v_permlane32_swap_b32_e32 v56, v58
	s_nop 1
	v_mov_b64_e32 v[64:65], v[128:129]
	v_mov_b64_e32 v[66:67], v[130:131]
	s_nop 3
	v_permlane32_swap_b32_e32 v65, v67
	v_permlane32_swap_b32_e32 v64, v66
	s_nop 1
	v_mfma_f32_32x32x16_bf16 v[20:35], v[56:59], v[40:43], v[20:35]
	v_mov_b64_e32 v[68:69], v[172:173]
	v_mov_b64_e32 v[70:71], v[174:175]
	s_nop 3
	v_permlane32_swap_b32_e32 v69, v71
	v_permlane32_swap_b32_e32 v68, v70
	s_nop 1
	v_mov_b64_e32 v[60:61], v[180:181]
	v_mov_b64_e32 v[62:63], v[182:183]
	s_nop 3
	v_permlane32_swap_b32_e32 v61, v63
	v_permlane32_swap_b32_e32 v60, v62
	s_nop 1
	v_mfma_f32_32x32x16_bf16 v[4:19], v[64:67], v[40:43], v[4:19]
	s_waitcnt vmcnt(16)
	v_mov_b64_e32 v[128:129], v[76:77]
	v_mov_b64_e32 v[130:131], v[78:79]
	s_nop 3
	v_permlane32_swap_b32_e32 v129, v131
	v_permlane32_swap_b32_e32 v128, v130
	s_nop 1
	v_mfma_f32_32x32x16_bf16 v[20:35], v[68:71], v[44:47], v[20:35]
	v_mov_b64_e32 v[112:113], v[88:89]
	v_mov_b64_e32 v[114:115], v[90:91]
	s_nop 3
	v_permlane32_swap_b32_e32 v113, v115
	v_permlane32_swap_b32_e32 v112, v114
	s_nop 1
	v_mov_b64_e32 v[124:125], v[80:81]
	v_mov_b64_e32 v[126:127], v[82:83]
	s_nop 3
	v_permlane32_swap_b32_e32 v125, v127
	v_permlane32_swap_b32_e32 v124, v126
	s_nop 1
	v_mfma_f32_32x32x16_bf16 v[4:19], v[60:63], v[44:47], v[4:19]
	s_waitcnt lgkmcnt(0)
	v_cndmask_b32_e32 v109, v167, v121, vcc
	v_cndmask_b32_e32 v108, v145, v120, vcc
	v_cndmask_b32_e32 v121, v204, v185, vcc
	v_cndmask_b32_e32 v120, v203, v184, vcc
	v_mov_b64_e32 v[104:105], v[188:189]
	v_mov_b64_e32 v[106:107], v[190:191]
	s_nop 3
	v_permlane32_swap_b32_e32 v105, v107
	v_permlane32_swap_b32_e32 v104, v106
	s_nop 1
	v_mov_b64_e32 v[116:117], v[192:193]
	v_mov_b64_e32 v[118:119], v[194:195]
	s_nop 3
	v_permlane32_swap_b32_e32 v117, v119
	v_permlane32_swap_b32_e32 v116, v118
	s_nop 1
	s_waitcnt lgkmcnt(0)
	v_mov_b64_e32 v[100:101], v[196:197]
	v_mov_b64_e32 v[102:103], v[198:199]
	s_nop 3
	v_permlane32_swap_b32_e32 v101, v103
	v_permlane32_swap_b32_e32 v100, v102
	s_nop 1
	v_cndmask_b32_e32 v111, v123, v167, vcc
	v_cndmask_b32_e32 v110, v122, v145, vcc
	v_cndmask_b32_e32 v123, v187, v204, vcc
	v_cndmask_b32_e32 v122, v186, v203, vcc
	v_mov_b64_e32 v[72:73], v[100:101]
	v_mov_b64_e32 v[88:89], v[116:117]
	v_mov_b64_e32 v[80:81], v[104:105]
	v_mov_b64_e32 v[96:97], v[120:121]
	v_mov_b64_e32 v[68:69], v[108:109]
	v_mov_b64_e32 v[84:85], v[124:125]
	v_mov_b64_e32 v[76:77], v[112:113]
	v_mov_b64_e32 v[92:93], v[128:129]
	v_mov_b64_e32 v[74:75], v[102:103]
	v_mov_b64_e32 v[90:91], v[118:119]
	v_mov_b64_e32 v[82:83], v[106:107]
	v_mov_b64_e32 v[98:99], v[122:123]
	v_mov_b64_e32 v[70:71], v[110:111]
	v_mov_b64_e32 v[86:87], v[126:127]
	v_mov_b64_e32 v[78:79], v[114:115]
	v_mov_b64_e32 v[94:95], v[130:131]
	s_cbranch_scc1 .LBB0_800
	v_cvt_pk_bf16_f32 v70, v20, v21
	v_cvt_pk_bf16_f32 v20, -v20, -v21
	v_cvt_pk_bf16_f32 v71, v22, v23
	v_cvt_pk_bf16_f32 v21, -v22, -v23
	v_cvt_pk_bf16_f32 v22, -v24, -v25
	v_lshlrev_b32_e32 v52, 16, v158
	v_and_b32_e32 v53, 0xffff0000, v158
	v_lshlrev_b32_e32 v54, 16, v159
	v_and_b32_e32 v55, 0xffff0000, v159
	v_lshlrev_b32_e32 v56, 16, v154
	v_and_b32_e32 v57, 0xffff0000, v154
	v_lshlrev_b32_e32 v58, 16, v155
	v_and_b32_e32 v59, 0xffff0000, v155
	v_lshlrev_b32_e32 v60, 16, v152
	v_and_b32_e32 v61, 0xffff0000, v152
	v_lshlrev_b32_e32 v62, 16, v153
	v_and_b32_e32 v63, 0xffff0000, v153
	v_lshlrev_b32_e32 v64, 16, v150
	v_and_b32_e32 v65, 0xffff0000, v150
	v_lshlrev_b32_e32 v66, 16, v151
	v_and_b32_e32 v67, 0xffff0000, v151
	v_cvt_pk_bf16_f32 v23, -v26, -v27
	v_lshlrev_b32_e32 v36, 16, v164
	v_and_b32_e32 v37, 0xffff0000, v164
	v_lshlrev_b32_e32 v38, 16, v165
	v_and_b32_e32 v39, 0xffff0000, v165
	v_lshlrev_b32_e32 v40, 16, v162
	v_and_b32_e32 v41, 0xffff0000, v162
	v_lshlrev_b32_e32 v42, 16, v163
	v_and_b32_e32 v43, 0xffff0000, v163
	v_lshlrev_b32_e32 v44, 16, v160
	v_and_b32_e32 v45, 0xffff0000, v160
	v_lshlrev_b32_e32 v46, 16, v161
	v_and_b32_e32 v47, 0xffff0000, v161
	v_lshlrev_b32_e32 v48, 16, v156
	v_and_b32_e32 v49, 0xffff0000, v156
	v_lshlrev_b32_e32 v50, 16, v157
	v_and_b32_e32 v51, 0xffff0000, v157
	v_mfma_f32_32x32x16_bf16 v[52:67], v[128:131], v[20:23], v[52:67]
	v_cvt_pk_bf16_f32 v72, v4, v5
	v_cvt_pk_bf16_f32 v4, -v4, -v5
	v_cvt_pk_bf16_f32 v73, v6, v7
	v_mfma_f32_32x32x16_bf16 v[36:51], v[120:123], v[20:23], v[36:51]
	v_cvt_pk_bf16_f32 v5, -v6, -v7
	v_cvt_pk_bf16_f32 v6, -v8, -v9
	v_cvt_pk_bf16_f32 v7, -v10, -v11
	s_or_b32 s4, s20, s17
	v_mfma_f32_32x32x16_bf16 v[52:67], v[124:127], v[4:7], v[52:67]
	s_or_b32 s4, s4, 0xfc
	s_ashr_i32 s5, s4, 31
	s_lshl_b64 s[14:15], s[4:5], 13
	v_lshl_add_u64 v[68:69], v[148:149], 0, s[14:15]
	global_store_dwordx2 v[68:69], v[70:71], off
	global_store_dwordx2 v[68:69], v[72:73], off offset:64
	v_cvt_pk_bf16_f32 v72, v8, v9
	v_mfma_f32_32x32x16_bf16 v[36:51], v[116:119], v[4:7], v[36:51]
	v_cvt_pk_bf16_f32 v4, -v28, -v29
	v_cvt_pk_bf16_f32 v5, -v30, -v31
	v_cvt_pk_bf16_f32 v6, -v32, -v33
	v_cvt_pk_bf16_f32 v7, -v34, -v35
	v_cvt_pk_bf16_f32 v8, -v12, -v13
	v_mfma_f32_32x32x16_bf16 v[52:67], v[112:115], v[4:7], v[52:67]
	v_cvt_pk_bf16_f32 v73, v10, v11
	v_cvt_pk_bf16_f32 v9, -v14, -v15
	v_cvt_pk_bf16_f32 v10, -v16, -v17
	v_mfma_f32_32x32x16_bf16 v[36:51], v[104:107], v[4:7], v[36:51]
	v_xor_b32_e32 v2, 0x80000000, v18
	v_xor_b32_e32 v11, 0x80000000, v19
	v_cvt_pk_bf16_f32 v11, v2, v11
	v_cvt_pk_bf16_f32 v70, v24, v25
	v_cvt_pk_bf16_f32 v71, v26, v27
	global_store_dwordx2 v[68:69], v[70:71], off offset:16
	global_store_dwordx2 v[68:69], v[72:73], off offset:80
	v_cvt_pk_bf16_f32 v70, v28, v29
	v_mfma_f32_32x32x16_bf16 v[52:67], v[108:111], v[8:11], v[52:67]
	v_cvt_pk_bf16_f32 v71, v30, v31
	v_cvt_pk_bf16_f32 v72, v12, v13
	v_cvt_pk_bf16_f32 v73, v14, v15
	global_store_dwordx2 v[68:69], v[70:71], off offset:32
	global_store_dwordx2 v[68:69], v[72:73], off offset:96
	v_cvt_pk_bf16_f32 v70, v32, v33
	v_cvt_pk_bf16_f32 v71, v34, v35
	v_lshl_add_u64 v[4:5], v[146:147], 0, s[14:15]
	v_mfma_f32_32x32x16_bf16 v[36:51], v[100:103], v[8:11], v[36:51]
	s_nop 2
	v_cvt_pk_bf16_f32 v6, v52, v53
	v_cvt_pk_bf16_f32 v7, v54, v55
	v_cvt_pk_bf16_f32 v72, v16, v17
	v_cvt_pk_bf16_f32 v73, v18, v19
	global_store_dwordx2 v[68:69], v[70:71], off offset:48
	global_store_dwordx2 v[68:69], v[72:73], off offset:112
	s_add_i32 s16, s16, s54
	s_cmp_lt_i32 s16, 64
	s_nop 0
	v_cvt_pk_bf16_f32 v8, v36, v37
	v_cvt_pk_bf16_f32 v9, v38, v39
	global_store_dwordx2 v[4:5], v[6:7], off
	global_store_dwordx2 v[4:5], v[8:9], off offset:64
	v_cvt_pk_bf16_f32 v6, v56, v57
	v_cvt_pk_bf16_f32 v7, v58, v59
	v_cvt_pk_bf16_f32 v8, v40, v41
	v_cvt_pk_bf16_f32 v9, v42, v43
	global_store_dwordx2 v[4:5], v[6:7], off offset:16
	global_store_dwordx2 v[4:5], v[8:9], off offset:80
	v_cvt_pk_bf16_f32 v6, v60, v61
	v_cvt_pk_bf16_f32 v7, v62, v63
	v_cvt_pk_bf16_f32 v8, v44, v45
	v_cvt_pk_bf16_f32 v9, v46, v47
	global_store_dwordx2 v[4:5], v[6:7], off offset:32
	global_store_dwordx2 v[4:5], v[8:9], off offset:96
	v_cvt_pk_bf16_f32 v6, v64, v65
	v_cvt_pk_bf16_f32 v7, v66, v67
	v_cvt_pk_bf16_f32 v8, v48, v49
	v_cvt_pk_bf16_f32 v9, v50, v51
	global_store_dwordx2 v[4:5], v[6:7], off offset:48
	global_store_dwordx2 v[4:5], v[8:9], off offset:112
	s_cbranch_scc1 .LBB0_799
